# strategy 7.12: per-lane ballot (v_cndmask + v_cmp_ne) after the fp8 K-loop barrier replaced by the equivalent s_andn2_b64 of the known mask, P10 and P11 loops
# speedup vs baseline: 1.0049x; 1.0049x over previous
.LBB0_1172:
	v_add_u32_e32 v14, 0x14000, v221
	ds_read_b128 v[18:21], v222
	ds_read_b128 v[22:25], v222 offset:1024
	ds_read_b128 v[26:29], v222 offset:2048
	ds_read_b128 v[30:33], v222 offset:3072
	ds_read_b128 v[2:5], v14
	ds_read_b128 v[6:9], v14 offset:1024
	ds_read_b128 v[10:13], v14 offset:2048
	ds_read_b128 v[14:17], v14 offset:3072
	v_lshl_add_u64 v[68:69], s[58:59], 0, v[208:209]
	s_add_i32 m0, s70, 0xc000
	s_waitcnt lgkmcnt(0)
	ds_read_b128 v[34:37], v223
	ds_read_b128 v[38:41], v223 offset:1024
	ds_read_b128 v[42:45], v223 offset:2048
	ds_read_b128 v[46:49], v223 offset:3072
	ds_read_b128 v[50:53], v223 offset:4096
	ds_read_b128 v[54:57], v223 offset:5120
	ds_read_b128 v[58:61], v223 offset:6144
	ds_read_b128 v[62:65], v223 offset:7168
	global_load_lds_dwordx4 v[68:69], off
	v_lshl_add_u64 v[68:69], s[58:59], 0, v[210:211]
	s_add_i32 m0, s70, 0xe000
	s_nop 0
	global_load_lds_dwordx4 v[68:69], off
	s_waitcnt vmcnt(8)
	s_waitcnt lgkmcnt(0)
	s_barrier
	s_setprio 1
	s_waitcnt lgkmcnt(0)
	v_mfma_scale_f32_16x16x128_f8f6f4 v[194:197], v[18:25], v[34:41], v[194:197], v220, v220 op_sel_hi:[0,0,0]
	v_mfma_scale_f32_16x16x128_f8f6f4 v[186:189], v[26:33], v[34:41], v[186:189], v220, v220 op_sel_hi:[0,0,0]
	v_mfma_scale_f32_16x16x128_f8f6f4 v[178:181], v[18:25], v[42:49], v[178:181], v220, v220 op_sel_hi:[0,0,0]
	v_mfma_scale_f32_16x16x128_f8f6f4 v[170:173], v[26:33], v[42:49], v[170:173], v220, v220 op_sel_hi:[0,0,0]
	v_mfma_scale_f32_16x16x128_f8f6f4 v[162:165], v[18:25], v[50:57], v[162:165], v220, v220 op_sel_hi:[0,0,0]
	v_mfma_scale_f32_16x16x128_f8f6f4 v[154:157], v[26:33], v[50:57], v[154:157], v220, v220 op_sel_hi:[0,0,0]
	v_mfma_scale_f32_16x16x128_f8f6f4 v[146:149], v[18:25], v[58:65], v[146:149], v220, v220 op_sel_hi:[0,0,0]
	v_mfma_scale_f32_16x16x128_f8f6f4 v[138:141], v[26:33], v[58:65], v[138:141], v220, v220 op_sel_hi:[0,0,0]
	s_setprio 0
	s_setprio 1
	v_mfma_scale_f32_16x16x128_f8f6f4 v[190:193], v[2:9], v[34:41], v[190:193], v220, v220 op_sel_hi:[0,0,0]
	v_mfma_scale_f32_16x16x128_f8f6f4 v[182:185], v[10:17], v[34:41], v[182:185], v220, v220 op_sel_hi:[0,0,0]
	v_mfma_scale_f32_16x16x128_f8f6f4 v[174:177], v[2:9], v[42:49], v[174:177], v220, v220 op_sel_hi:[0,0,0]
	v_mfma_scale_f32_16x16x128_f8f6f4 v[166:169], v[10:17], v[42:49], v[166:169], v220, v220 op_sel_hi:[0,0,0]
	v_mfma_scale_f32_16x16x128_f8f6f4 v[158:161], v[2:9], v[50:57], v[158:161], v220, v220 op_sel_hi:[0,0,0]
	v_mfma_scale_f32_16x16x128_f8f6f4 v[150:153], v[10:17], v[50:57], v[150:153], v220, v220 op_sel_hi:[0,0,0]
	v_mfma_scale_f32_16x16x128_f8f6f4 v[142:145], v[2:9], v[58:65], v[142:145], v220, v220 op_sel_hi:[0,0,0]
	v_mfma_scale_f32_16x16x128_f8f6f4 v[134:137], v[10:17], v[58:65], v[134:137], v220, v220 op_sel_hi:[0,0,0]
	s_setprio 0
	s_barrier
	s_andn2_b64 s[6:7], exec, s[8:9]
	s_andn2_b64 vcc, exec, s[8:9]
	s_cbranch_vccnz .LBB0_1174
	ds_read_b128 v[34:37], v223 offset:16384
	ds_read_b128 v[38:41], v223 offset:17408
	ds_read_b128 v[42:45], v223 offset:18432
	ds_read_b128 v[46:49], v223 offset:19456
	ds_read_b128 v[50:53], v223 offset:20480
	ds_read_b128 v[54:57], v223 offset:21504
	ds_read_b128 v[58:61], v223 offset:22528
	ds_read_b128 v[62:65], v223 offset:23552

.LBB0_1296:
	v_add_u32_e32 v2, 0x10000, v232
	v_add_u32_e32 v14, 0x14000, v232
	ds_read_b128 v[18:21], v2
	ds_read_b128 v[22:25], v2 offset:1024
	ds_read_b128 v[26:29], v2 offset:2048
	ds_read_b128 v[30:33], v2 offset:3072
	ds_read_b128 v[2:5], v14
	ds_read_b128 v[6:9], v14 offset:1024
	ds_read_b128 v[10:13], v14 offset:2048
	ds_read_b128 v[14:17], v14 offset:3072
	v_lshl_add_u64 v[68:69], s[64:65], 0, v[210:211]
	s_add_i32 m0, s63, 0xc000
	s_waitcnt lgkmcnt(0)
	ds_read_b128 v[34:37], v233
	ds_read_b128 v[38:41], v233 offset:1024
	ds_read_b128 v[42:45], v233 offset:2048
	ds_read_b128 v[46:49], v233 offset:3072
	ds_read_b128 v[50:53], v233 offset:4096
	ds_read_b128 v[54:57], v233 offset:5120
	ds_read_b128 v[58:61], v233 offset:6144
	ds_read_b128 v[62:65], v233 offset:7168
	global_load_lds_dwordx4 v[68:69], off
	v_lshl_add_u64 v[68:69], s[64:65], 0, v[212:213]
	s_add_i32 m0, s63, 0xe000
	s_nop 0
	global_load_lds_dwordx4 v[68:69], off
	s_waitcnt vmcnt(8)
	s_waitcnt lgkmcnt(0)
	s_barrier
	s_setprio 1
	s_waitcnt lgkmcnt(0)
	v_mfma_scale_f32_16x16x128_f8f6f4 v[194:197], v[18:25], v[34:41], v[194:197], v231, v231 op_sel_hi:[0,0,0]
	v_mfma_scale_f32_16x16x128_f8f6f4 v[190:193], v[26:33], v[34:41], v[190:193], v231, v231 op_sel_hi:[0,0,0]
	v_mfma_scale_f32_16x16x128_f8f6f4 v[186:189], v[18:25], v[42:49], v[186:189], v231, v231 op_sel_hi:[0,0,0]
	v_mfma_scale_f32_16x16x128_f8f6f4 v[182:185], v[26:33], v[42:49], v[182:185], v231, v231 op_sel_hi:[0,0,0]
	v_mfma_scale_f32_16x16x128_f8f6f4 v[166:169], v[18:25], v[50:57], v[166:169], v231, v231 op_sel_hi:[0,0,0]
	v_mfma_scale_f32_16x16x128_f8f6f4 v[158:161], v[26:33], v[50:57], v[158:161], v231, v231 op_sel_hi:[0,0,0]
	v_mfma_scale_f32_16x16x128_f8f6f4 v[154:157], v[18:25], v[58:65], v[154:157], v231, v231 op_sel_hi:[0,0,0]
	v_mfma_scale_f32_16x16x128_f8f6f4 v[150:153], v[26:33], v[58:65], v[150:153], v231, v231 op_sel_hi:[0,0,0]
	s_setprio 0
	s_setprio 1
	v_mfma_scale_f32_16x16x128_f8f6f4 v[178:181], v[2:9], v[34:41], v[178:181], v231, v231 op_sel_hi:[0,0,0]
	v_mfma_scale_f32_16x16x128_f8f6f4 v[174:177], v[10:17], v[34:41], v[174:177], v231, v231 op_sel_hi:[0,0,0]
	v_mfma_scale_f32_16x16x128_f8f6f4 v[170:173], v[2:9], v[42:49], v[170:173], v231, v231 op_sel_hi:[0,0,0]
	v_mfma_scale_f32_16x16x128_f8f6f4 v[162:165], v[10:17], v[42:49], v[162:165], v231, v231 op_sel_hi:[0,0,0]
	v_mfma_scale_f32_16x16x128_f8f6f4 v[146:149], v[2:9], v[50:57], v[146:149], v231, v231 op_sel_hi:[0,0,0]
	v_mfma_scale_f32_16x16x128_f8f6f4 v[142:145], v[10:17], v[50:57], v[142:145], v231, v231 op_sel_hi:[0,0,0]
	v_mfma_scale_f32_16x16x128_f8f6f4 v[138:141], v[2:9], v[58:65], v[138:141], v231, v231 op_sel_hi:[0,0,0]
	v_mfma_scale_f32_16x16x128_f8f6f4 v[134:137], v[10:17], v[58:65], v[134:137], v231, v231 op_sel_hi:[0,0,0]
	s_setprio 0
	s_barrier
	s_andn2_b64 s[10:11], exec, s[8:9]
	s_andn2_b64 vcc, exec, s[8:9]
	s_cbranch_vccnz .LBB0_1298
	ds_read_b128 v[34:37], v233 offset:16384
	ds_read_b128 v[38:41], v233 offset:17408
	ds_read_b128 v[42:45], v233 offset:18432
	ds_read_b128 v[46:49], v233 offset:19456
	ds_read_b128 v[50:53], v233 offset:20480
	ds_read_b128 v[54:57], v233 offset:21504
	ds_read_b128 v[58:61], v233 offset:22528
	ds_read_b128 v[62:65], v233 offset:23552
